# attention-phase balance v2: conversion quota -5 (bid<16), layer0: -4 (bid<32), +3 (bid>=192)
# speedup vs baseline: 1.0115x; 1.0025x over previous
; __global__ void __launch_bounds__(512, 2) mk_fwd(Args a) {
;     ...
;         if (IN(pb + 5) && (c.bid & 1) == 0) { if (l == 0) mod_items(a, c, 1); bg_take(a, c, l == 0 ? 26 : 24); }
;         if (EN(5) && IN(pb + 5)) for (int rep = 0; rep < NREP(5); ++rep) { phase_attn(a, c, l, last); }
;         if (IN(pb + 5) && (c.bid & 1) == 1) { bg_take(a, c, l == 0 ? 26 : 24); if (l == 0) mod_items(a, c, 1); }
.Lbal1_a:
	s_cmp_lt_u32 s14, 25
	s_cbranch_scc1 .Lbal1_c
	s_cmp_lt_u32 s90, 32
	s_cbranch_scc0 .Lbal1_b
	s_add_i32 s14, s14, -4
.Lbal1_b:
	s_cmp_gt_u32 s90, 191
	s_cbranch_scc0 .Lbal1_c
	s_add_i32 s14, s14, 3

; __global__ void __launch_bounds__(512, 2) mk_fwd(Args a) {
;     ...
;         if (IN(pb + 5) && (c.bid & 1) == 0) { if (l == 0) mod_items(a, c, 1); bg_take(a, c, l == 0 ? 26 : 24); }
;         if (EN(5) && IN(pb + 5)) for (int rep = 0; rep < NREP(5); ++rep) { phase_attn(a, c, l, last); }
;         if (IN(pb + 5) && (c.bid & 1) == 1) { bg_take(a, c, l == 0 ? 26 : 24); if (l == 0) mod_items(a, c, 1); }
.Lbal2_a:
	s_cmp_lt_u32 s10, 25
	s_cbranch_scc1 .Lbal2_c
	s_cmp_lt_u32 s90, 32
	s_cbranch_scc0 .Lbal2_b
	s_add_i32 s10, s10, -4
.Lbal2_b:
	s_cmp_gt_u32 s90, 191
	s_cbranch_scc0 .Lbal2_c
	s_add_i32 s10, s10, 3
